# plus layer-0 conversion: prefix-max of positions computed by one 6-step scan instead of 128 dependent load+shuffle steps
# speedup vs baseline: 1.0087x; 1.0015x over previous
; __device__ __forceinline__ int shi(int v, int src_lane) { return __builtin_amdgcn_ds_bpermute(src_lane << 2, v); }
; __device__ __forceinline__ void phase_conv(LAS unsigned char* lds, int wv, int l) {
;     ...
;         if (gw == 1) {
;             int run = -2147483647 - 1;
;             for (int t = 0; t < S / 64; ++t) { int v = pos[t * 64 + F.lane];
; #pragma unroll
;                 for (int o = 1; o < 64; o <<= 1) { const int w_ = shi(v, F.lane ^ o); v = v > w_ ? v : w_; }
;                 run = run > v ? run : v; if (F.lane == 0) ((int*)(F.ctl + CW_PMAX))[t] = run; }
;         }
.LBB0_193:
	s_andn2_b64 vcc, exec, s[16:17]
	s_cbranch_vccnz .LBB0_204
	v_lshlrev_b32_e32 v2, 8, v12
	v_mov_b32_e32 v3, v31
	v_lshl_add_u64 v[2:3], s[14:15], 0, v[2:3]
	s_mov_b64 s[2:3], 0x4000
	v_lshl_add_u64 v[4:5], v[2:3], 0, s[2:3]
	global_load_dwordx4 v[32:35], v[2:3], off
	global_load_dwordx4 v[36:39], v[2:3], off offset:16
	global_load_dwordx4 v[40:43], v[2:3], off offset:32
	global_load_dwordx4 v[44:47], v[2:3], off offset:48
	global_load_dwordx4 v[48:51], v[2:3], off offset:64
	global_load_dwordx4 v[52:55], v[2:3], off offset:80
	global_load_dwordx4 v[56:59], v[2:3], off offset:96
	global_load_dwordx4 v[60:63], v[2:3], off offset:112
	global_load_dwordx4 v[64:67], v[2:3], off offset:128
	global_load_dwordx4 v[68:71], v[2:3], off offset:144
	global_load_dwordx4 v[72:75], v[2:3], off offset:160
	global_load_dwordx4 v[76:79], v[2:3], off offset:176
	global_load_dwordx4 v[80:83], v[2:3], off offset:192
	global_load_dwordx4 v[84:87], v[2:3], off offset:208
	global_load_dwordx4 v[88:91], v[2:3], off offset:224
	global_load_dwordx4 v[92:95], v[2:3], off offset:240
	s_waitcnt vmcnt(0)
	v_max3_i32 v13, v32, v33, v34
	v_max3_i32 v13, v13, v35, v36
	v_max3_i32 v13, v13, v37, v38
	v_max3_i32 v13, v13, v39, v40
	v_max3_i32 v13, v13, v41, v42
	v_max3_i32 v13, v13, v43, v44
	v_max3_i32 v13, v13, v45, v46
	v_max3_i32 v13, v13, v47, v48
	v_max3_i32 v13, v13, v49, v50
	v_max3_i32 v13, v13, v51, v52
	v_max3_i32 v13, v13, v53, v54
	v_max3_i32 v13, v13, v55, v56
	v_max3_i32 v13, v13, v57, v58
	v_max3_i32 v13, v13, v59, v60
	v_max3_i32 v13, v13, v61, v62
	v_max3_i32 v13, v13, v63, v64
	v_max3_i32 v13, v13, v65, v66
	v_max3_i32 v13, v13, v67, v68
	v_max3_i32 v13, v13, v69, v70
	v_max3_i32 v13, v13, v71, v72
	v_max3_i32 v13, v13, v73, v74
	v_max3_i32 v13, v13, v75, v76
	v_max3_i32 v13, v13, v77, v78
	v_max3_i32 v13, v13, v79, v80
	v_max3_i32 v13, v13, v81, v82
	v_max3_i32 v13, v13, v83, v84
	v_max3_i32 v13, v13, v85, v86
	v_max3_i32 v13, v13, v87, v88
	v_max3_i32 v13, v13, v89, v90
	v_max3_i32 v13, v13, v91, v92
	v_max3_i32 v13, v13, v93, v94
	v_max_i32_e32 v13, v13, v95
	s_nop 0
	global_load_dwordx4 v[32:35], v[4:5], off
	global_load_dwordx4 v[36:39], v[4:5], off offset:16
	global_load_dwordx4 v[40:43], v[4:5], off offset:32
	global_load_dwordx4 v[44:47], v[4:5], off offset:48
	global_load_dwordx4 v[48:51], v[4:5], off offset:64
	global_load_dwordx4 v[52:55], v[4:5], off offset:80
	global_load_dwordx4 v[56:59], v[4:5], off offset:96
	global_load_dwordx4 v[60:63], v[4:5], off offset:112
	global_load_dwordx4 v[64:67], v[4:5], off offset:128
	global_load_dwordx4 v[68:71], v[4:5], off offset:144
	global_load_dwordx4 v[72:75], v[4:5], off offset:160
	global_load_dwordx4 v[76:79], v[4:5], off offset:176
	global_load_dwordx4 v[80:83], v[4:5], off offset:192
	global_load_dwordx4 v[84:87], v[4:5], off offset:208
	global_load_dwordx4 v[88:91], v[4:5], off offset:224
	global_load_dwordx4 v[92:95], v[4:5], off offset:240
	s_waitcnt vmcnt(0)
	v_max3_i32 v14, v32, v33, v34
	v_max3_i32 v14, v14, v35, v36
	v_max3_i32 v14, v14, v37, v38
	v_max3_i32 v14, v14, v39, v40
	v_max3_i32 v14, v14, v41, v42
	v_max3_i32 v14, v14, v43, v44
	v_max3_i32 v14, v14, v45, v46
	v_max3_i32 v14, v14, v47, v48
	v_max3_i32 v14, v14, v49, v50
	v_max3_i32 v14, v14, v51, v52
	v_max3_i32 v14, v14, v53, v54
	v_max3_i32 v14, v14, v55, v56
	v_max3_i32 v14, v14, v57, v58
	v_max3_i32 v14, v14, v59, v60
	v_max3_i32 v14, v14, v61, v62
	v_max3_i32 v14, v14, v63, v64
	v_max3_i32 v14, v14, v65, v66
	v_max3_i32 v14, v14, v67, v68
	v_max3_i32 v14, v14, v69, v70
	v_max3_i32 v14, v14, v71, v72
	v_max3_i32 v14, v14, v73, v74
	v_max3_i32 v14, v14, v75, v76
	v_max3_i32 v14, v14, v77, v78
	v_max3_i32 v14, v14, v79, v80
	v_max3_i32 v14, v14, v81, v82
	v_max3_i32 v14, v14, v83, v84
	v_max3_i32 v14, v14, v85, v86
	v_max3_i32 v14, v14, v87, v88
	v_max3_i32 v14, v14, v89, v90
	v_max3_i32 v14, v14, v91, v92
	v_max3_i32 v14, v14, v93, v94
	v_max_i32_e32 v14, v14, v95
	v_lshlrev_b32_e32 v1, 2, v12
	v_subrev_u32_e32 v6, 4, v1
	ds_bpermute_b32 v7, v6, v13
	ds_bpermute_b32 v8, v6, v14
	v_cmp_le_u32_e32 vcc, 1, v12
	s_waitcnt lgkmcnt(0)
	v_max_i32_e32 v7, v7, v13
	v_max_i32_e32 v8, v8, v14
	v_cndmask_b32_e32 v13, v13, v7, vcc
	v_cndmask_b32_e32 v14, v14, v8, vcc
	v_subrev_u32_e32 v6, 8, v1
	ds_bpermute_b32 v7, v6, v13
	ds_bpermute_b32 v8, v6, v14
	v_cmp_le_u32_e32 vcc, 2, v12
	s_waitcnt lgkmcnt(0)
	v_max_i32_e32 v7, v7, v13
	v_max_i32_e32 v8, v8, v14
	v_cndmask_b32_e32 v13, v13, v7, vcc
	v_cndmask_b32_e32 v14, v14, v8, vcc
	v_subrev_u32_e32 v6, 16, v1
	ds_bpermute_b32 v7, v6, v13
	ds_bpermute_b32 v8, v6, v14
	v_cmp_le_u32_e32 vcc, 4, v12
	s_waitcnt lgkmcnt(0)
	v_max_i32_e32 v7, v7, v13
	v_max_i32_e32 v8, v8, v14
	v_cndmask_b32_e32 v13, v13, v7, vcc
	v_cndmask_b32_e32 v14, v14, v8, vcc
	v_subrev_u32_e32 v6, 32, v1
	ds_bpermute_b32 v7, v6, v13
	ds_bpermute_b32 v8, v6, v14
	v_cmp_le_u32_e32 vcc, 8, v12
	s_waitcnt lgkmcnt(0)
	v_max_i32_e32 v7, v7, v13
	v_max_i32_e32 v8, v8, v14
	v_cndmask_b32_e32 v13, v13, v7, vcc
	v_cndmask_b32_e32 v14, v14, v8, vcc
	v_subrev_u32_e32 v6, 64, v1
	ds_bpermute_b32 v7, v6, v13
	ds_bpermute_b32 v8, v6, v14
	v_cmp_le_u32_e32 vcc, 16, v12
	s_waitcnt lgkmcnt(0)
	v_max_i32_e32 v7, v7, v13
	v_max_i32_e32 v8, v8, v14
	v_cndmask_b32_e32 v13, v13, v7, vcc
	v_cndmask_b32_e32 v14, v14, v8, vcc
	v_subrev_u32_e32 v6, 128, v1
	ds_bpermute_b32 v7, v6, v13
	ds_bpermute_b32 v8, v6, v14
	v_cmp_le_u32_e32 vcc, 32, v12
	s_waitcnt lgkmcnt(0)
	v_max_i32_e32 v7, v7, v13
	v_max_i32_e32 v8, v8, v14
	v_cndmask_b32_e32 v13, v13, v7, vcc
	v_cndmask_b32_e32 v14, v14, v8, vcc
	s_nop 1
	v_readlane_b32 s2, v13, 63
	v_add_u32_e32 v0, 0x2a00, v1
	s_nop 1
	v_max_i32_e32 v14, s2, v14
	global_store_dword v0, v13, s[76:77]
	global_store_dword v0, v14, s[76:77] offset:256
